# gate (sigmoid to u8) epilogue of the fp8 projection: scale and -log2e folded into one multiply, the max(.,1) replaced by a clamp on the fma that forms (1+e)/255
# speedup vs baseline: 1.0057x; 1.0057x over previous
.LBB0_476:
	s_add_u32 s14, s40, 0.5
	s_addc_u32 s15, s41, 0
	s_add_i32 s33, s22, 0x18000
	s_or_b32 s21, s68, 0x80
	s_mov_b32 s6, s10
	s_mov_b32 s7, s11
	s_mov_b32 m0, s33
	s_add_i32 s34, s22, 0x1a000
	s_waitcnt vmcnt(2)
	s_barrier
	buffer_load_dwordx4 v1, s[4:7], s21 offen lds
	s_mov_b32 m0, s34
	s_add_i32 s35, s22, 0x8000
	buffer_load_dwordx4 v130, s[4:7], s21 offen lds
	s_or_b32 s21, s67, 0x80
	s_mov_b32 m0, s35
	s_add_i32 s38, s22, 0xa000
	buffer_load_dwordx4 v131, s[8:11], s21 offen lds
	s_mov_b32 m0, s38
	s_add_i32 s39, s22, 0x1c000
	buffer_load_dwordx4 v132, s[8:11], s21 offen lds
	s_or_b32 s21, s68, 0x40080
	s_mov_b32 m0, s39
	s_add_i32 s46, s22, 0x1e000
	buffer_load_dwordx4 v1, s[4:7], s21 offen lds
	s_mov_b32 m0, s46
	v_and_b32_e32 v134, 15, v2
	buffer_load_dwordx4 v130, s[4:7], s21 offen lds
	s_waitcnt vmcnt(14)
	v_mul_f32_e32 v133, 0x3c000000, v3
	v_mul_f32_e32 v254, 0xbfb8aa3b, v133
	v_bfe_u32 v135, v2, 4, 2
	v_lshlrev_b32_e32 v3, 6, v134
	v_lshlrev_b32_e32 v2, 2, v2
	s_and_b32 s6, s19, 3
	v_lshl_or_b32 v3, v135, 4, v3
	s_lshl_b32 s7, s20, 13
	v_and_b32_e32 v2, 32, v2
	v_bitop3_b32 v4, v3, s7, v2 bitop3:0xde
	s_lshl_b32 s7, s6, 12
	s_add_i32 s47, s22, 0xc000
	s_cmpk_lt_u32 s18, 0x100
	v_bitop3_b32 v2, v3, s7, v2 bitop3:0xde
	s_waitcnt vmcnt(6)
	s_cselect_b64 s[18:19], -1, 0
	s_lshl_b32 s7, s20, 12
	s_lshl_b32 s6, s6, 10
	s_or_b32 s48, s6, s7
	v_add_u32_e32 v2, 0, v2
	s_or_b32 s49, s48, 0x80
	s_or_b32 s50, s48, 0x100
	s_or_b32 s51, s48, 0x180
	s_or_b32 s52, s48, 0x200
	s_or_b32 s53, s48, 0x280
	s_or_b32 s54, s48, 0x300
	s_or_b32 s55, s48, 0x380
	s_add_i32 s56, s22, 0xe000
	v_add_u32_e32 v136, 0x10000, v2
	v_add_u32_e32 v137, 0x14000, v2
	v_add_u32_e32 v138, 0, v4
	v_add_u32_e32 v139, 0x18000, v2
	v_add_u32_e32 v140, 0x1c000, v2
	v_mov_b32_e32 v141, 0x3b808081
	s_mov_b32 s57, 0xc0c0400
	s_mov_b32 s58, 0x4000c0c
	s_barrier
	s_branch .LBB0_479

.LBB0_492:
	v_mul_f32_e32 v118, v254, v118
	v_mul_f32_e32 v119, v254, v119
	v_mul_f32_e32 v120, v254, v120
	v_mul_f32_e32 v121, v254, v121
	v_exp_f32_e32 v118, v118
	v_exp_f32_e32 v119, v119
	v_exp_f32_e32 v120, v120
	v_exp_f32_e32 v121, v121
	v_fma_f32 v118, v118, v141, v141 clamp
	v_fma_f32 v119, v119, v141, v141 clamp
	v_fma_f32 v120, v120, v141, v141 clamp
	v_fma_f32 v121, v121, v141, v141 clamp
	v_rcp_f32_e32 v118, v118
	v_rcp_f32_e32 v119, v119
	v_rcp_f32_e32 v120, v120
	v_rcp_f32_e32 v121, v121
	v_mul_f32_e32 v102, v254, v102
	v_mul_f32_e32 v103, v254, v103
	v_mul_f32_e32 v104, v254, v104
	v_mul_f32_e32 v105, v254, v105
	v_mul_f32_e32 v128, v254, v128
	v_mul_f32_e32 v129, v254, v129
	v_exp_f32_e32 v102, v102
	v_exp_f32_e32 v103, v103
	v_exp_f32_e32 v104, v104
	v_exp_f32_e32 v105, v105
	v_exp_f32_e32 v128, v128
	v_exp_f32_e32 v129, v129
	v_mul_f32_e32 v114, v254, v114
	v_mov_b32_e32 v142, v135
	v_mov_b32_e32 v143, v134
	v_mul_f32_e32 v126, v254, v126
	v_add_f32_e32 v118, 0x4b400000, v118
	v_add_f32_e32 v119, 0x4b400000, v119
	v_add_f32_e32 v120, 0x4b400000, v120
	v_add_f32_e32 v121, 0x4b400000, v121
	v_perm_b32 v118, v119, v118, s57
	v_perm_b32 v119, v121, v120, s58
	v_exp_f32_e32 v120, v114
	v_mul_f32_e32 v114, v254, v115
	v_mul_f32_e32 v116, v254, v116
	v_mul_f32_e32 v117, v254, v117
	v_fma_f32 v102, v102, v141, v141 clamp
	v_fma_f32 v103, v103, v141, v141 clamp
	v_fma_f32 v104, v104, v141, v141 clamp
	v_fma_f32 v105, v105, v141, v141 clamp
	v_lshl_add_u32 v142, v142, 4, v143
	v_exp_f32_e32 v143, v126
	v_mul_f32_e32 v126, v254, v127
	v_rcp_f32_e32 v102, v102
	v_rcp_f32_e32 v103, v103
	v_rcp_f32_e32 v104, v104
	v_rcp_f32_e32 v105, v105
	v_fma_f32 v128, v128, v141, v141 clamp
	v_fma_f32 v129, v129, v141, v141 clamp
	v_exp_f32_e32 v115, v114
	v_exp_f32_e32 v116, v116
	v_exp_f32_e32 v117, v117
	v_exp_f32_e32 v127, v126
	v_rcp_f32_e32 v128, v128
	v_rcp_f32_e32 v129, v129
	v_mul_f32_e32 v98, v254, v98
	v_or_b32_e32 v114, v119, v118
	v_fma_f32 v118, v120, v141, v141 clamp
	v_fma_f32 v115, v115, v141, v141 clamp
	v_fma_f32 v116, v116, v141, v141 clamp
	v_fma_f32 v117, v117, v141, v141 clamp
	v_add_f32_e32 v102, 0x4b400000, v102
	v_add_f32_e32 v103, 0x4b400000, v103
	v_add_f32_e32 v104, 0x4b400000, v104
	v_add_f32_e32 v105, 0x4b400000, v105
	v_fma_f32 v143, v143, v141, v141 clamp
	v_fma_f32 v127, v127, v141, v141 clamp
	v_mul_f32_e32 v122, v254, v122
	v_rcp_f32_e32 v118, v118
	v_rcp_f32_e32 v115, v115
	v_rcp_f32_e32 v116, v116
	v_rcp_f32_e32 v117, v117
	v_perm_b32 v102, v103, v102, s57
	v_perm_b32 v103, v105, v104, s58
	v_exp_f32_e32 v104, v98
	v_mul_f32_e32 v98, v254, v99
	v_mul_f32_e32 v100, v254, v100
	v_mul_f32_e32 v101, v254, v101
	v_rcp_f32_e32 v143, v143
	v_rcp_f32_e32 v127, v127
	v_add_f32_e32 v128, 0x4b400000, v128
	v_add_f32_e32 v129, 0x4b400000, v129
	v_perm_b32 v128, v129, v128, s58
	v_exp_f32_e32 v129, v122
	v_mul_f32_e32 v122, v254, v123
	v_mul_f32_e32 v124, v254, v124
	v_mul_f32_e32 v125, v254, v125
	v_exp_f32_e32 v99, v98
	v_exp_f32_e32 v100, v100
	v_exp_f32_e32 v101, v101
	s_lshr_b32 s6, s64, 3
	s_mulk_i32 s6, 0x42
	v_exp_f32_e32 v123, v122
	v_exp_f32_e32 v124, v124
	v_exp_f32_e32 v125, v125
	v_mul_f32_e32 v86, v254, v86
	v_mul_f32_e32 v87, v254, v87
	v_mul_f32_e32 v88, v254, v88
	v_mul_f32_e32 v89, v254, v89
	s_add_i32 s6, s6, s63
	v_add_f32_e32 v118, 0x4b400000, v118
	v_add_f32_e32 v115, 0x4b400000, v115
	v_add_f32_e32 v116, 0x4b400000, v116
	v_add_f32_e32 v117, 0x4b400000, v117
	s_and_b32 s7, s64, 7
	s_lshl_b32 s6, s6, 3
	v_add_u32_e32 v126, s48, v142
	v_add_f32_e32 v143, 0x4b400000, v143
	v_add_f32_e32 v127, 0x4b400000, v127
	v_perm_b32 v115, v115, v118, s57
	v_perm_b32 v116, v117, v116, s58
	v_mul_f32_e32 v112, v254, v112
	v_mul_f32_e32 v113, v254, v113
	v_or_b32_e32 v98, v103, v102
	v_fma_f32 v102, v104, v141, v141 clamp
	v_fma_f32 v99, v99, v141, v141 clamp
	v_fma_f32 v100, v100, v141, v141 clamp
	v_fma_f32 v101, v101, v141, v141 clamp
	v_exp_f32_e32 v86, v86
	v_exp_f32_e32 v87, v87
	v_exp_f32_e32 v88, v88
	v_exp_f32_e32 v89, v89
	s_or_b32 s6, s6, s7
	v_perm_b32 v127, v127, v143, s57
	v_or_b32_e32 v115, v116, v115
	v_add_u32_e32 v116, 64, v126
	v_rcp_f32_e32 v102, v102
	v_rcp_f32_e32 v99, v99
	v_rcp_f32_e32 v100, v100
	v_rcp_f32_e32 v101, v101
	s_ashr_i32 s7, s6, 31
	v_or_b32_e32 v122, v128, v127
	v_fma_f32 v127, v129, v141, v141 clamp
	v_fma_f32 v123, v123, v141, v141 clamp
	v_fma_f32 v124, v124, v141, v141 clamp
	v_fma_f32 v125, v125, v141, v141 clamp
	v_ashrrev_i32_e32 v117, 31, v116
	v_exp_f32_e32 v112, v112
	v_exp_f32_e32 v113, v113
	s_lshl_b64 s[6:7], s[6:7], 16
	v_rcp_f32_e32 v127, v127
	v_rcp_f32_e32 v123, v123
	v_rcp_f32_e32 v124, v124
	v_rcp_f32_e32 v125, v125
	v_lshl_add_u64 v[116:117], v[116:117], 3, s[14:15]
	v_mul_f32_e32 v110, v254, v110
	v_lshl_add_u64 v[116:117], v[116:117], 0, s[6:7]
	v_fma_f32 v86, v86, v141, v141 clamp
	v_fma_f32 v87, v87, v141, v141 clamp
	v_fma_f32 v88, v88, v141, v141 clamp
	v_fma_f32 v89, v89, v141, v141 clamp
	global_store_dwordx2 v[116:117], v[114:115], off nt
	v_exp_f32_e32 v114, v110
	v_mul_f32_e32 v110, v254, v111
	v_rcp_f32_e32 v86, v86
	v_rcp_f32_e32 v87, v87
	v_rcp_f32_e32 v88, v88
	v_rcp_f32_e32 v89, v89
	v_mul_f32_e32 v70, v254, v70
	v_mul_f32_e32 v71, v254, v71
	v_mul_f32_e32 v72, v254, v72
	v_mul_f32_e32 v73, v254, v73
	v_fma_f32 v112, v112, v141, v141 clamp
	v_fma_f32 v113, v113, v141, v141 clamp
	v_add_f32_e32 v102, 0x4b400000, v102
	v_add_f32_e32 v99, 0x4b400000, v99
	v_add_f32_e32 v100, 0x4b400000, v100
	v_add_f32_e32 v101, 0x4b400000, v101
	v_exp_f32_e32 v111, v110
	v_add_u32_e32 v110, s49, v142
	v_rcp_f32_e32 v112, v112
	v_rcp_f32_e32 v113, v113
	v_perm_b32 v99, v99, v102, s57
	v_perm_b32 v100, v101, v100, s58
	v_mul_f32_e32 v96, v254, v96
	v_mul_f32_e32 v97, v254, v97
	v_exp_f32_e32 v70, v70
	v_exp_f32_e32 v71, v71
	v_exp_f32_e32 v72, v72
	v_exp_f32_e32 v73, v73
	v_add_f32_e32 v127, 0x4b400000, v127
	v_add_f32_e32 v123, 0x4b400000, v123
	v_add_f32_e32 v124, 0x4b400000, v124
	v_add_f32_e32 v125, 0x4b400000, v125
	v_or_b32_e32 v99, v100, v99
	v_add_u32_e32 v100, 64, v110
	v_perm_b32 v123, v123, v127, s57
	v_perm_b32 v124, v125, v124, s58
	v_ashrrev_i32_e32 v127, 31, v126
	v_ashrrev_i32_e32 v101, 31, v100
	v_exp_f32_e32 v96, v96
	v_exp_f32_e32 v97, v97
	v_mul_f32_e32 v82, v254, v82
	v_or_b32_e32 v123, v124, v123
	v_lshl_add_u64 v[124:125], v[126:127], 3, s[14:15]
	v_lshl_add_u64 v[100:101], v[100:101], 3, s[14:15]
	v_mul_f32_e32 v94, v254, v94
	v_add_f32_e32 v86, 0x4b400000, v86
	v_add_f32_e32 v87, 0x4b400000, v87
	v_add_f32_e32 v88, 0x4b400000, v88
	v_add_f32_e32 v89, 0x4b400000, v89
	v_lshl_add_u64 v[124:125], v[124:125], 0, s[6:7]
	v_fma_f32 v114, v114, v141, v141 clamp
	v_fma_f32 v111, v111, v141, v141 clamp
	v_mul_f32_e32 v106, v254, v106
	v_lshl_add_u64 v[100:101], v[100:101], 0, s[6:7]
	v_perm_b32 v86, v87, v86, s57
	v_perm_b32 v87, v89, v88, s58
	v_exp_f32_e32 v88, v82
	v_mul_f32_e32 v82, v254, v83
	v_mul_f32_e32 v84, v254, v84
	v_mul_f32_e32 v85, v254, v85
	v_fma_f32 v70, v70, v141, v141 clamp
	v_fma_f32 v71, v71, v141, v141 clamp
	v_fma_f32 v72, v72, v141, v141 clamp
	v_fma_f32 v73, v73, v141, v141 clamp
	global_store_dwordx2 v[124:125], v[122:123], off nt
	v_rcp_f32_e32 v114, v114
	v_rcp_f32_e32 v111, v111
	v_add_f32_e32 v112, 0x4b400000, v112
	v_add_f32_e32 v113, 0x4b400000, v113
	global_store_dwordx2 v[100:101], v[98:99], off nt
	v_exp_f32_e32 v98, v94
	v_mul_f32_e32 v94, v254, v95
	v_rcp_f32_e32 v70, v70
	v_rcp_f32_e32 v71, v71
	v_rcp_f32_e32 v72, v72
	v_rcp_f32_e32 v73, v73
	v_perm_b32 v112, v113, v112, s58
	v_exp_f32_e32 v113, v106
	v_mul_f32_e32 v106, v254, v107
	v_mul_f32_e32 v108, v254, v108
	v_mul_f32_e32 v109, v254, v109
	v_fma_f32 v96, v96, v141, v141 clamp
	v_fma_f32 v97, v97, v141, v141 clamp
	v_exp_f32_e32 v83, v82
	v_exp_f32_e32 v84, v84
	v_exp_f32_e32 v85, v85
	v_exp_f32_e32 v95, v94
	v_rcp_f32_e32 v96, v96
	v_rcp_f32_e32 v97, v97
	v_exp_f32_e32 v107, v106
	v_exp_f32_e32 v108, v108
	v_exp_f32_e32 v109, v109
	v_mul_f32_e32 v66, v254, v66
	v_add_f32_e32 v114, 0x4b400000, v114
	v_add_f32_e32 v111, 0x4b400000, v111
	v_or_b32_e32 v82, v87, v86
	v_fma_f32 v86, v88, v141, v141 clamp
	v_fma_f32 v83, v83, v141, v141 clamp
	v_fma_f32 v84, v84, v141, v141 clamp
	v_fma_f32 v85, v85, v141, v141 clamp
	v_add_f32_e32 v70, 0x4b400000, v70
	v_add_f32_e32 v71, 0x4b400000, v71
	v_add_f32_e32 v72, 0x4b400000, v72
	v_add_f32_e32 v73, 0x4b400000, v73
	v_perm_b32 v111, v111, v114, s57
	v_fma_f32 v98, v98, v141, v141 clamp
	v_fma_f32 v95, v95, v141, v141 clamp
	v_mul_f32_e32 v90, v254, v90
	v_rcp_f32_e32 v86, v86
	v_rcp_f32_e32 v83, v83
	v_rcp_f32_e32 v84, v84
	v_rcp_f32_e32 v85, v85
	v_perm_b32 v70, v71, v70, s57
	v_perm_b32 v71, v73, v72, s58
	v_exp_f32_e32 v72, v66
	v_mul_f32_e32 v66, v254, v67
	v_mul_f32_e32 v68, v254, v68
	v_mul_f32_e32 v69, v254, v69
	v_or_b32_e32 v106, v112, v111
	v_fma_f32 v111, v113, v141, v141 clamp
	v_fma_f32 v107, v107, v141, v141 clamp
	v_fma_f32 v108, v108, v141, v141 clamp
	v_fma_f32 v109, v109, v141, v141 clamp
	v_rcp_f32_e32 v98, v98
	v_rcp_f32_e32 v95, v95
	v_add_f32_e32 v96, 0x4b400000, v96
	v_add_f32_e32 v97, 0x4b400000, v97
	v_rcp_f32_e32 v111, v111
	v_rcp_f32_e32 v107, v107
	v_rcp_f32_e32 v108, v108
	v_rcp_f32_e32 v109, v109
	v_perm_b32 v96, v97, v96, s58
	v_exp_f32_e32 v97, v90
	v_mul_f32_e32 v90, v254, v91
	v_mul_f32_e32 v92, v254, v92
	v_mul_f32_e32 v93, v254, v93
	v_exp_f32_e32 v67, v66
	v_exp_f32_e32 v68, v68
	v_exp_f32_e32 v69, v69
	v_exp_f32_e32 v91, v90
	v_exp_f32_e32 v92, v92
	v_exp_f32_e32 v93, v93
	v_add_f32_e32 v86, 0x4b400000, v86
	v_add_f32_e32 v83, 0x4b400000, v83
	v_add_f32_e32 v84, 0x4b400000, v84
	v_add_f32_e32 v85, 0x4b400000, v85
	v_add_u32_e32 v94, s50, v142
	v_add_f32_e32 v98, 0x4b400000, v98
	v_add_f32_e32 v95, 0x4b400000, v95
	v_perm_b32 v83, v83, v86, s57
	v_perm_b32 v84, v85, v84, s58
	v_or_b32_e32 v66, v71, v70
	v_fma_f32 v70, v72, v141, v141 clamp
	v_fma_f32 v67, v67, v141, v141 clamp
	v_fma_f32 v68, v68, v141, v141 clamp
	v_fma_f32 v69, v69, v141, v141 clamp
	v_add_f32_e32 v111, 0x4b400000, v111
	v_add_f32_e32 v107, 0x4b400000, v107
	v_add_f32_e32 v108, 0x4b400000, v108
	v_add_f32_e32 v109, 0x4b400000, v109
	v_perm_b32 v95, v95, v98, s57
	v_or_b32_e32 v83, v84, v83
	v_add_u32_e32 v84, 64, v94
	v_rcp_f32_e32 v70, v70
	v_rcp_f32_e32 v67, v67
	v_rcp_f32_e32 v68, v68
	v_rcp_f32_e32 v69, v69
	v_perm_b32 v107, v107, v111, s57
	v_perm_b32 v108, v109, v108, s58
	v_ashrrev_i32_e32 v111, 31, v110
	v_or_b32_e32 v90, v96, v95
	v_fma_f32 v95, v97, v141, v141 clamp
	v_fma_f32 v91, v91, v141, v141 clamp
	v_fma_f32 v92, v92, v141, v141 clamp
	v_fma_f32 v93, v93, v141, v141 clamp
	v_ashrrev_i32_e32 v85, 31, v84
	v_or_b32_e32 v107, v108, v107
	v_lshl_add_u64 v[108:109], v[110:111], 3, s[14:15]
	v_rcp_f32_e32 v95, v95
	v_rcp_f32_e32 v91, v91
	v_rcp_f32_e32 v92, v92
	v_rcp_f32_e32 v93, v93
	v_lshl_add_u64 v[84:85], v[84:85], 3, s[14:15]
	v_mul_f32_e32 v78, v254, v78
	v_lshl_add_u64 v[108:109], v[108:109], 0, s[6:7]
	v_lshl_add_u64 v[84:85], v[84:85], 0, s[6:7]
	global_store_dwordx2 v[108:109], v[106:107], off nt
	global_store_dwordx2 v[84:85], v[82:83], off nt
	v_exp_f32_e32 v82, v78
	v_mul_f32_e32 v78, v254, v79
	v_add_f32_e32 v70, 0x4b400000, v70
	v_add_f32_e32 v67, 0x4b400000, v67
	v_add_f32_e32 v68, 0x4b400000, v68
	v_add_f32_e32 v69, 0x4b400000, v69
	v_exp_f32_e32 v79, v78
	v_add_u32_e32 v78, s51, v142
	v_perm_b32 v67, v67, v70, s57
	v_perm_b32 v68, v69, v68, s58
	v_mul_f32_e32 v64, v254, v64
	v_mul_f32_e32 v65, v254, v65
	v_add_f32_e32 v95, 0x4b400000, v95
	v_add_f32_e32 v91, 0x4b400000, v91
	v_add_f32_e32 v92, 0x4b400000, v92
	v_add_f32_e32 v93, 0x4b400000, v93
	v_or_b32_e32 v67, v68, v67
	v_add_u32_e32 v68, 64, v78
	v_perm_b32 v91, v91, v95, s57
	v_perm_b32 v92, v93, v92, s58
	v_ashrrev_i32_e32 v95, 31, v94
	v_ashrrev_i32_e32 v69, 31, v68
	v_exp_f32_e32 v64, v64
	v_exp_f32_e32 v65, v65
	v_or_b32_e32 v91, v92, v91
	v_lshl_add_u64 v[92:93], v[94:95], 3, s[14:15]
	v_lshl_add_u64 v[68:69], v[68:69], 3, s[14:15]
	v_mul_f32_e32 v62, v254, v62
	v_lshl_add_u64 v[92:93], v[92:93], 0, s[6:7]
	v_lshl_add_u64 v[68:69], v[68:69], 0, s[6:7]
	global_store_dwordx2 v[92:93], v[90:91], off nt
	global_store_dwordx2 v[68:69], v[66:67], off nt
	v_exp_f32_e32 v66, v62
	v_mul_f32_e32 v62, v254, v63
	v_fma_f32 v64, v64, v141, v141 clamp
	v_fma_f32 v65, v65, v141, v141 clamp
	v_exp_f32_e32 v63, v62
	v_rcp_f32_e32 v64, v64
	v_rcp_f32_e32 v65, v65
	v_fma_f32 v66, v66, v141, v141 clamp
	v_fma_f32 v63, v63, v141, v141 clamp
	v_mul_f32_e32 v54, v254, v54
	v_rcp_f32_e32 v66, v66
	v_rcp_f32_e32 v63, v63
	v_add_f32_e32 v64, 0x4b400000, v64
	v_add_f32_e32 v65, 0x4b400000, v65
	v_perm_b32 v64, v65, v64, s58
	v_exp_f32_e32 v65, v54
	v_mul_f32_e32 v54, v254, v55
	v_mul_f32_e32 v56, v254, v56
	v_mul_f32_e32 v57, v254, v57
	v_exp_f32_e32 v55, v54
	v_exp_f32_e32 v56, v56
	v_exp_f32_e32 v57, v57
	v_add_f32_e32 v66, 0x4b400000, v66
	v_add_f32_e32 v63, 0x4b400000, v63
	v_perm_b32 v63, v63, v66, s57
	v_or_b32_e32 v54, v64, v63
	v_fma_f32 v63, v65, v141, v141 clamp
	v_fma_f32 v55, v55, v141, v141 clamp
	v_fma_f32 v56, v56, v141, v141 clamp
	v_fma_f32 v57, v57, v141, v141 clamp
	v_rcp_f32_e32 v63, v63
	v_rcp_f32_e32 v55, v55
	v_rcp_f32_e32 v56, v56
	v_rcp_f32_e32 v57, v57
	v_add_u32_e32 v62, s52, v142
	v_add_f32_e32 v63, 0x4b400000, v63
	v_add_f32_e32 v55, 0x4b400000, v55
	v_add_f32_e32 v56, 0x4b400000, v56
	v_add_f32_e32 v57, 0x4b400000, v57
	v_perm_b32 v55, v55, v63, s57
	v_perm_b32 v56, v57, v56, s58
	v_ashrrev_i32_e32 v63, 31, v62
	v_or_b32_e32 v55, v56, v55
	v_lshl_add_u64 v[56:57], v[62:63], 3, s[14:15]
	v_lshl_add_u64 v[56:57], v[56:57], 0, s[6:7]
	v_mul_f32_e32 v58, v254, v58
	v_mul_f32_e32 v59, v254, v59
	global_store_dwordx2 v[56:57], v[54:55], off nt
	v_mul_f32_e32 v56, v254, v60
	v_mul_f32_e32 v57, v254, v61
	v_mul_f32_e32 v80, v254, v80
	v_mul_f32_e32 v81, v254, v81
	v_exp_f32_e32 v58, v58
	v_exp_f32_e32 v59, v59
	v_exp_f32_e32 v56, v56
	v_exp_f32_e32 v57, v57
	v_exp_f32_e32 v80, v80
	v_exp_f32_e32 v81, v81
	v_fma_f32 v54, v58, v141, v141 clamp
	v_fma_f32 v55, v59, v141, v141 clamp
	v_fma_f32 v56, v56, v141, v141 clamp
	v_fma_f32 v57, v57, v141, v141 clamp
	v_rcp_f32_e32 v54, v54
	v_rcp_f32_e32 v55, v55
	v_rcp_f32_e32 v56, v56
	v_rcp_f32_e32 v57, v57
	v_fma_f32 v80, v80, v141, v141 clamp
	v_fma_f32 v81, v81, v141, v141 clamp
	v_rcp_f32_e32 v80, v80
	v_rcp_f32_e32 v81, v81
	v_mul_f32_e32 v50, v254, v50
	v_add_f32_e32 v54, 0x4b400000, v54
	v_add_f32_e32 v55, 0x4b400000, v55
	v_add_f32_e32 v56, 0x4b400000, v56
	v_add_f32_e32 v57, 0x4b400000, v57
	v_fma_f32 v82, v82, v141, v141 clamp
	v_fma_f32 v79, v79, v141, v141 clamp
	v_mul_f32_e32 v74, v254, v74
	v_perm_b32 v54, v55, v54, s57
	v_perm_b32 v55, v57, v56, s58
	v_exp_f32_e32 v56, v50
	v_mul_f32_e32 v50, v254, v51
	v_mul_f32_e32 v52, v254, v52
	v_mul_f32_e32 v53, v254, v53
	v_rcp_f32_e32 v82, v82
	v_rcp_f32_e32 v79, v79
	v_add_f32_e32 v80, 0x4b400000, v80
	v_add_f32_e32 v81, 0x4b400000, v81
	v_perm_b32 v80, v81, v80, s58
	v_exp_f32_e32 v81, v74
	v_mul_f32_e32 v74, v254, v75
	v_mul_f32_e32 v76, v254, v76
	v_mul_f32_e32 v77, v254, v77
	v_exp_f32_e32 v51, v50
	v_exp_f32_e32 v52, v52
	v_exp_f32_e32 v53, v53
	v_exp_f32_e32 v75, v74
	v_exp_f32_e32 v76, v76
	v_exp_f32_e32 v77, v77
	v_add_f32_e32 v82, 0x4b400000, v82
	v_add_f32_e32 v79, 0x4b400000, v79
	v_or_b32_e32 v50, v55, v54
	v_fma_f32 v54, v56, v141, v141 clamp
	v_fma_f32 v51, v51, v141, v141 clamp
	v_fma_f32 v52, v52, v141, v141 clamp
	v_fma_f32 v53, v53, v141, v141 clamp
	v_perm_b32 v79, v79, v82, s57
	v_rcp_f32_e32 v54, v54
	v_rcp_f32_e32 v51, v51
	v_rcp_f32_e32 v52, v52
	v_rcp_f32_e32 v53, v53
	v_or_b32_e32 v74, v80, v79
	v_fma_f32 v79, v81, v141, v141 clamp
	v_fma_f32 v75, v75, v141, v141 clamp
	v_fma_f32 v76, v76, v141, v141 clamp
	v_fma_f32 v77, v77, v141, v141 clamp
	v_rcp_f32_e32 v79, v79
	v_rcp_f32_e32 v75, v75
	v_rcp_f32_e32 v76, v76
	v_rcp_f32_e32 v77, v77
	v_add_f32_e32 v54, 0x4b400000, v54
	v_add_f32_e32 v51, 0x4b400000, v51
	v_add_f32_e32 v52, 0x4b400000, v52
	v_add_f32_e32 v53, 0x4b400000, v53
	v_perm_b32 v51, v51, v54, s57
	v_perm_b32 v52, v53, v52, s58
	v_mul_f32_e32 v48, v254, v48
	v_mul_f32_e32 v49, v254, v49
	v_add_f32_e32 v79, 0x4b400000, v79
	v_add_f32_e32 v75, 0x4b400000, v75
	v_add_f32_e32 v76, 0x4b400000, v76
	v_add_f32_e32 v77, 0x4b400000, v77
	v_or_b32_e32 v51, v52, v51
	v_add_u32_e32 v52, 64, v62
	v_perm_b32 v75, v75, v79, s57
	v_perm_b32 v76, v77, v76, s58
	v_ashrrev_i32_e32 v79, 31, v78
	v_ashrrev_i32_e32 v53, 31, v52
	v_exp_f32_e32 v48, v48
	v_exp_f32_e32 v49, v49
	v_or_b32_e32 v75, v76, v75
	v_lshl_add_u64 v[76:77], v[78:79], 3, s[14:15]
	v_lshl_add_u64 v[52:53], v[52:53], 3, s[14:15]
	v_mul_f32_e32 v46, v254, v46
	v_lshl_add_u64 v[76:77], v[76:77], 0, s[6:7]
	v_lshl_add_u64 v[52:53], v[52:53], 0, s[6:7]
	global_store_dwordx2 v[76:77], v[74:75], off nt
	global_store_dwordx2 v[52:53], v[50:51], off nt
	v_exp_f32_e32 v50, v46
	v_mul_f32_e32 v46, v254, v47
	v_fma_f32 v48, v48, v141, v141 clamp
	v_fma_f32 v49, v49, v141, v141 clamp
	v_exp_f32_e32 v47, v46
	v_rcp_f32_e32 v48, v48
	v_rcp_f32_e32 v49, v49
	v_fma_f32 v50, v50, v141, v141 clamp
	v_fma_f32 v47, v47, v141, v141 clamp
	v_mul_f32_e32 v34, v254, v34
	v_rcp_f32_e32 v50, v50
	v_rcp_f32_e32 v47, v47
	v_add_f32_e32 v48, 0x4b400000, v48
	v_add_f32_e32 v49, 0x4b400000, v49
	v_perm_b32 v48, v49, v48, s58
	v_exp_f32_e32 v49, v34
	v_mul_f32_e32 v34, v254, v35
	v_mul_f32_e32 v36, v254, v36
	v_mul_f32_e32 v37, v254, v37
	v_exp_f32_e32 v35, v34
	v_exp_f32_e32 v36, v36
	v_exp_f32_e32 v37, v37
	v_add_f32_e32 v50, 0x4b400000, v50
	v_add_f32_e32 v47, 0x4b400000, v47
	v_perm_b32 v47, v47, v50, s57
	v_or_b32_e32 v34, v48, v47
	v_fma_f32 v47, v49, v141, v141 clamp
	v_fma_f32 v35, v35, v141, v141 clamp
	v_fma_f32 v36, v36, v141, v141 clamp
	v_fma_f32 v37, v37, v141, v141 clamp
	v_rcp_f32_e32 v47, v47
	v_rcp_f32_e32 v35, v35
	v_rcp_f32_e32 v36, v36
	v_rcp_f32_e32 v37, v37
	v_add_u32_e32 v46, s53, v142
	v_add_f32_e32 v47, 0x4b400000, v47
	v_add_f32_e32 v35, 0x4b400000, v35
	v_add_f32_e32 v36, 0x4b400000, v36
	v_add_f32_e32 v37, 0x4b400000, v37
	v_perm_b32 v35, v35, v47, s57
	v_perm_b32 v36, v37, v36, s58
	v_ashrrev_i32_e32 v47, 31, v46
	v_or_b32_e32 v35, v36, v35
	v_lshl_add_u64 v[36:37], v[46:47], 3, s[14:15]
	v_lshl_add_u64 v[36:37], v[36:37], 0, s[6:7]
	v_mul_f32_e32 v42, v254, v42
	v_mul_f32_e32 v43, v254, v43
	global_store_dwordx2 v[36:37], v[34:35], off nt
	v_mul_f32_e32 v36, v254, v44
	v_mul_f32_e32 v37, v254, v45
	v_exp_f32_e32 v42, v42
	v_exp_f32_e32 v43, v43
	v_exp_f32_e32 v36, v36
	v_exp_f32_e32 v37, v37
	v_fma_f32 v34, v42, v141, v141 clamp
	v_fma_f32 v35, v43, v141, v141 clamp
	v_fma_f32 v36, v36, v141, v141 clamp
	v_fma_f32 v37, v37, v141, v141 clamp
	v_rcp_f32_e32 v34, v34
	v_rcp_f32_e32 v35, v35
	v_rcp_f32_e32 v36, v36
	v_rcp_f32_e32 v37, v37
	v_add_f32_e32 v34, 0x4b400000, v34
	v_add_f32_e32 v35, 0x4b400000, v35
	v_add_f32_e32 v36, 0x4b400000, v36
	v_add_f32_e32 v37, 0x4b400000, v37
	v_perm_b32 v34, v35, v34, s57
	v_perm_b32 v35, v37, v36, s58
	v_mul_f32_e32 v36, v254, v38
	v_mul_f32_e32 v37, v254, v39
	v_exp_f32_e32 v36, v36
	v_exp_f32_e32 v37, v37
	v_or_b32_e32 v34, v35, v34
	v_mul_f32_e32 v38, v254, v41
	v_fma_f32 v35, v36, v141, v141 clamp
	v_fma_f32 v36, v37, v141, v141 clamp
	v_mul_f32_e32 v37, v254, v40
	v_exp_f32_e32 v37, v37
	v_exp_f32_e32 v38, v38
	v_rcp_f32_e32 v35, v35
	v_rcp_f32_e32 v36, v36
	v_fma_f32 v37, v37, v141, v141 clamp
	v_fma_f32 v38, v38, v141, v141 clamp
	v_rcp_f32_e32 v37, v37
	v_rcp_f32_e32 v38, v38
	v_add_f32_e32 v35, 0x4b400000, v35
	v_add_f32_e32 v36, 0x4b400000, v36
	v_add_f32_e32 v37, 0x4b400000, v37
	v_add_f32_e32 v38, 0x4b400000, v38
	v_perm_b32 v35, v36, v35, s57
	v_perm_b32 v36, v38, v37, s58
	v_mul_f32_e32 v28, v254, v28
	v_mul_f32_e32 v29, v254, v29
	v_or_b32_e32 v35, v36, v35
	v_add_u32_e32 v36, 64, v46
	v_ashrrev_i32_e32 v37, 31, v36
	v_exp_f32_e32 v28, v28
	v_exp_f32_e32 v29, v29
	v_lshl_add_u64 v[36:37], v[36:37], 3, s[14:15]
	v_mul_f32_e32 v26, v254, v26
	v_lshl_add_u64 v[36:37], v[36:37], 0, s[6:7]
	global_store_dwordx2 v[36:37], v[34:35], off nt
	v_exp_f32_e32 v34, v26
	v_mul_f32_e32 v26, v254, v27
	v_fma_f32 v28, v28, v141, v141 clamp
	v_fma_f32 v29, v29, v141, v141 clamp
	v_exp_f32_e32 v27, v26
	v_rcp_f32_e32 v28, v28
	v_rcp_f32_e32 v29, v29
	v_fma_f32 v34, v34, v141, v141 clamp
	v_fma_f32 v27, v27, v141, v141 clamp
	v_mul_f32_e32 v18, v254, v18
	v_rcp_f32_e32 v34, v34
	v_rcp_f32_e32 v27, v27
	v_add_f32_e32 v28, 0x4b400000, v28
	v_add_f32_e32 v29, 0x4b400000, v29
	v_perm_b32 v28, v29, v28, s58
	v_exp_f32_e32 v29, v18
	v_mul_f32_e32 v18, v254, v19
	v_mul_f32_e32 v20, v254, v20
	v_mul_f32_e32 v21, v254, v21
	v_exp_f32_e32 v19, v18
	v_exp_f32_e32 v20, v20
	v_exp_f32_e32 v21, v21
	v_add_f32_e32 v34, 0x4b400000, v34
	v_add_f32_e32 v27, 0x4b400000, v27
	v_perm_b32 v27, v27, v34, s57
	v_or_b32_e32 v18, v28, v27
	v_fma_f32 v27, v29, v141, v141 clamp
	v_fma_f32 v19, v19, v141, v141 clamp
	v_fma_f32 v20, v20, v141, v141 clamp
	v_fma_f32 v21, v21, v141, v141 clamp
	v_rcp_f32_e32 v27, v27
	v_rcp_f32_e32 v19, v19
	v_rcp_f32_e32 v20, v20
	v_rcp_f32_e32 v21, v21
	v_add_u32_e32 v26, s54, v142
	v_add_f32_e32 v27, 0x4b400000, v27
	v_add_f32_e32 v19, 0x4b400000, v19
	v_add_f32_e32 v20, 0x4b400000, v20
	v_add_f32_e32 v21, 0x4b400000, v21
	v_perm_b32 v19, v19, v27, s57
	v_perm_b32 v20, v21, v20, s58
	v_ashrrev_i32_e32 v27, 31, v26
	v_or_b32_e32 v19, v20, v19
	v_lshl_add_u64 v[20:21], v[26:27], 3, s[14:15]
	v_lshl_add_u64 v[20:21], v[20:21], 0, s[6:7]
	v_mul_f32_e32 v27, v254, v30
	v_mul_f32_e32 v28, v254, v31
	global_store_dwordx2 v[20:21], v[18:19], off nt
	v_mul_f32_e32 v20, v254, v32
	v_mul_f32_e32 v21, v254, v33
	v_exp_f32_e32 v27, v27
	v_exp_f32_e32 v28, v28
	v_exp_f32_e32 v20, v20
	v_exp_f32_e32 v21, v21
	v_fma_f32 v18, v27, v141, v141 clamp
	v_fma_f32 v19, v28, v141, v141 clamp
	v_fma_f32 v20, v20, v141, v141 clamp
	v_fma_f32 v21, v21, v141, v141 clamp
	v_rcp_f32_e32 v18, v18
	v_rcp_f32_e32 v19, v19
	v_rcp_f32_e32 v20, v20
	v_rcp_f32_e32 v21, v21
	v_add_f32_e32 v18, 0x4b400000, v18
	v_add_f32_e32 v19, 0x4b400000, v19
	v_add_f32_e32 v20, 0x4b400000, v20
	v_add_f32_e32 v21, 0x4b400000, v21
	v_perm_b32 v18, v19, v18, s57
	v_perm_b32 v19, v21, v20, s58
	v_mul_f32_e32 v20, v254, v22
	v_mul_f32_e32 v21, v254, v23
	v_exp_f32_e32 v20, v20
	v_exp_f32_e32 v21, v21
	v_or_b32_e32 v18, v19, v18
	v_mul_f32_e32 v22, v254, v25
	v_fma_f32 v19, v20, v141, v141 clamp
	v_fma_f32 v20, v21, v141, v141 clamp
	v_mul_f32_e32 v21, v254, v24
	v_exp_f32_e32 v21, v21
	v_exp_f32_e32 v22, v22
	v_rcp_f32_e32 v19, v19
	v_rcp_f32_e32 v20, v20
	v_fma_f32 v21, v21, v141, v141 clamp
	v_fma_f32 v22, v22, v141, v141 clamp
	v_rcp_f32_e32 v21, v21
	v_rcp_f32_e32 v22, v22
	v_add_f32_e32 v19, 0x4b400000, v19
	v_add_f32_e32 v20, 0x4b400000, v20
	v_add_f32_e32 v21, 0x4b400000, v21
	v_add_f32_e32 v22, 0x4b400000, v22
	v_perm_b32 v19, v20, v19, s57
	v_perm_b32 v20, v22, v21, s58
	v_mul_f32_e32 v12, v254, v12
	v_mul_f32_e32 v13, v254, v13
	v_or_b32_e32 v19, v20, v19
	v_add_u32_e32 v20, 64, v26
	v_ashrrev_i32_e32 v21, 31, v20
	v_exp_f32_e32 v12, v12
	v_exp_f32_e32 v13, v13
	v_lshl_add_u64 v[20:21], v[20:21], 3, s[14:15]
	v_mul_f32_e32 v10, v254, v10
	v_lshl_add_u64 v[20:21], v[20:21], 0, s[6:7]
	global_store_dwordx2 v[20:21], v[18:19], off nt
	v_exp_f32_e32 v18, v10
	v_mul_f32_e32 v10, v254, v11
	v_fma_f32 v12, v12, v141, v141 clamp
	v_fma_f32 v13, v13, v141, v141 clamp
	v_exp_f32_e32 v11, v10
	v_rcp_f32_e32 v12, v12
	v_rcp_f32_e32 v13, v13
	v_fma_f32 v18, v18, v141, v141 clamp
	v_fma_f32 v11, v11, v141, v141 clamp
	v_mul_f32_e32 v2, v254, v2
	v_rcp_f32_e32 v18, v18
	v_rcp_f32_e32 v11, v11
	v_add_f32_e32 v12, 0x4b400000, v12
	v_add_f32_e32 v13, 0x4b400000, v13
	v_perm_b32 v12, v13, v12, s58
	v_exp_f32_e32 v13, v2
	v_mul_f32_e32 v2, v254, v3
	v_mul_f32_e32 v4, v254, v4
	v_mul_f32_e32 v5, v254, v5
	v_exp_f32_e32 v3, v2
	v_exp_f32_e32 v4, v4
	v_exp_f32_e32 v5, v5
	v_add_f32_e32 v18, 0x4b400000, v18
	v_add_f32_e32 v11, 0x4b400000, v11
	v_perm_b32 v11, v11, v18, s57
	v_or_b32_e32 v2, v12, v11
	v_fma_f32 v11, v13, v141, v141 clamp
	v_fma_f32 v3, v3, v141, v141 clamp
	v_fma_f32 v4, v4, v141, v141 clamp
	v_fma_f32 v5, v5, v141, v141 clamp
	v_rcp_f32_e32 v11, v11
	v_rcp_f32_e32 v3, v3
	v_rcp_f32_e32 v4, v4
	v_rcp_f32_e32 v5, v5
	v_add_u32_e32 v10, s55, v142
	v_add_f32_e32 v11, 0x4b400000, v11
	v_add_f32_e32 v3, 0x4b400000, v3
	v_add_f32_e32 v4, 0x4b400000, v4
	v_add_f32_e32 v5, 0x4b400000, v5
	v_perm_b32 v3, v3, v11, s57
	v_perm_b32 v4, v5, v4, s58
	v_ashrrev_i32_e32 v11, 31, v10
	v_or_b32_e32 v3, v4, v3
	v_lshl_add_u64 v[4:5], v[10:11], 3, s[14:15]
	v_lshl_add_u64 v[4:5], v[4:5], 0, s[6:7]
	v_mul_f32_e32 v11, v254, v14
	v_mul_f32_e32 v12, v254, v15
	global_store_dwordx2 v[4:5], v[2:3], off nt
	v_mul_f32_e32 v4, v254, v16
	v_mul_f32_e32 v5, v254, v17
	v_exp_f32_e32 v11, v11
	v_exp_f32_e32 v12, v12
	v_exp_f32_e32 v4, v4
	v_exp_f32_e32 v5, v5
	v_fma_f32 v2, v11, v141, v141 clamp
	v_fma_f32 v3, v12, v141, v141 clamp
	v_fma_f32 v4, v4, v141, v141 clamp
	v_fma_f32 v5, v5, v141, v141 clamp
	v_rcp_f32_e32 v2, v2
	v_rcp_f32_e32 v3, v3
	v_rcp_f32_e32 v4, v4
	v_rcp_f32_e32 v5, v5
	v_add_f32_e32 v2, 0x4b400000, v2
	v_add_f32_e32 v3, 0x4b400000, v3
	v_add_f32_e32 v4, 0x4b400000, v4
	v_add_f32_e32 v5, 0x4b400000, v5
	v_perm_b32 v2, v3, v2, s57
	v_perm_b32 v3, v5, v4, s58
	v_mul_f32_e32 v4, v254, v6
	v_mul_f32_e32 v5, v254, v7
	v_exp_f32_e32 v4, v4
	v_exp_f32_e32 v5, v5
	v_or_b32_e32 v2, v3, v2
	v_mul_f32_e32 v6, v254, v9
	v_fma_f32 v3, v4, v141, v141 clamp
	v_fma_f32 v4, v5, v141, v141 clamp
	v_mul_f32_e32 v5, v254, v8
	v_exp_f32_e32 v5, v5
	v_exp_f32_e32 v6, v6
	v_rcp_f32_e32 v3, v3
	v_rcp_f32_e32 v4, v4
	v_fma_f32 v5, v5, v141, v141 clamp
	v_fma_f32 v6, v6, v141, v141 clamp
	v_rcp_f32_e32 v5, v5
	v_rcp_f32_e32 v6, v6
	v_add_f32_e32 v3, 0x4b400000, v3
	v_add_f32_e32 v4, 0x4b400000, v4
	v_add_f32_e32 v5, 0x4b400000, v5
	v_add_f32_e32 v6, 0x4b400000, v6
	v_perm_b32 v3, v4, v3, s57
	v_perm_b32 v4, v6, v5, s58
	v_or_b32_e32 v3, v4, v3
	v_add_u32_e32 v4, 64, v10
	v_ashrrev_i32_e32 v5, 31, v4
	v_lshl_add_u64 v[4:5], v[4:5], 3, s[14:15]
	v_lshl_add_u64 v[4:5], v[4:5], 0, s[6:7]
	s_andn2_b64 vcc, exec, s[20:21]
	s_mov_b64 s[6:7], -1
	global_store_dwordx2 v[4:5], v[2:3], off nt
	s_cbranch_vccnz .LBB0_478
	s_andn2_b64 vcc, exec, s[12:13]
	s_cbranch_vccnz .LBB0_477
	s_barrier
	s_branch .LBB0_477
